# MoE K-loops: the weight loads and activation LDS-DMA pieces are issued two MFMAs later inside each MFMA segment (same even spacing)
# speedup vs baseline: 1.0001x; 1.0001x over previous
.LBB0_1327:
	ds_read_b128 v[202:205], v180 offset:0
	ds_read_b128 v[206:209], v180 offset:0x2000
	ds_read_b128 v[210:213], v180 offset:0x4000
	ds_read_b128 v[214:217], v180 offset:0x6000
	ds_read_b128 v[218:221], v180 offset:0x8000
	ds_read_b128 v[222:225], v182 offset:0
	ds_read_b128 v[226:229], v178 offset:0x800
	ds_read_b128 v[230:233], v182 offset:0x2000
	ds_read_b128 v[234:237], v178 offset:0x2800
	s_waitcnt lgkmcnt(9)
	s_nop 1
	v_mfma_f32_16x16x32_bf16 v[168:171], v[68:71], v[92:95], v[168:171]
	v_mfma_f32_16x16x32_bf16 v[164:167], v[72:75], v[92:95], v[164:167]
	v_mfma_f32_16x16x32_bf16 v[160:163], v[80:83], v[92:95], v[160:163]
	v_mfma_f32_16x16x32_bf16 v[92:95], v[84:87], v[92:95], v[156:159]
	s_add_i32 s15, s3, 0xfffbd000
	buffer_load_dwordx4 v[24:27], v173, s[8:11], s15 offen
	v_mfma_f32_16x16x32_bf16 v[152:155], v[68:71], v[76:79], v[152:155]
	v_mfma_f32_16x16x32_bf16 v[148:151], v[72:75], v[76:79], v[148:151]
	v_mfma_f32_16x16x32_bf16 v[144:147], v[80:83], v[76:79], v[144:147]
	v_mfma_f32_16x16x32_bf16 v[76:79], v[84:87], v[76:79], v[140:143]
	v_mfma_f32_16x16x32_bf16 v[136:139], v[68:71], v[64:67], v[136:139]
	s_add_i32 s64, s3, 0xfffbe000
	buffer_load_dwordx4 v[32:35], v173, s[8:11], s64 offen
	v_mfma_f32_16x16x32_bf16 v[132:135], v[72:75], v[64:67], v[132:135]
	v_mfma_f32_16x16x32_bf16 v[128:131], v[80:83], v[64:67], v[128:131]
	v_mfma_f32_16x16x32_bf16 v[64:67], v[84:87], v[64:67], v[124:127]
	v_mfma_f32_16x16x32_bf16 v[120:123], v[68:71], v[60:63], v[120:123]
	v_mfma_f32_16x16x32_bf16 v[116:119], v[72:75], v[60:63], v[116:119]
	s_add_i32 s15, s3, 0xfffbf000
	buffer_load_dwordx4 v[20:23], v173, s[8:11], s15 offen
	v_mfma_f32_16x16x32_bf16 v[112:115], v[80:83], v[60:63], v[112:115]
	v_mfma_f32_16x16x32_bf16 v[60:63], v[84:87], v[60:63], v[108:111]
	v_mfma_f32_16x16x32_bf16 v[68:71], v[68:71], v[56:59], v[104:107]
	v_mfma_f32_16x16x32_bf16 v[72:75], v[72:75], v[56:59], v[100:103]
	v_mfma_f32_16x16x32_bf16 v[80:83], v[80:83], v[56:59], v[96:99]
	s_add_i32 s64, s3, 0xfffc0000
	buffer_load_dwordx4 v[28:31], v173, s[8:11], s64 offen
	v_mfma_f32_16x16x32_bf16 v[56:59], v[84:87], v[56:59], v[88:91]
	s_waitcnt vmcnt(4)
	v_cvt_pk_bf16_f32 v36, v242, v246
	v_cvt_pk_bf16_f32 v37, v250, v188
	ds_write_b64 v197, v[36:37]
	v_cvt_pk_bf16_f32 v36, v243, v247
	v_cvt_pk_bf16_f32 v37, v251, v189
	ds_write_b64 v198, v[36:37]
	v_cvt_pk_bf16_f32 v36, v244, v248
	v_cvt_pk_bf16_f32 v37, v252, v190
	ds_write_b64 v199, v[36:37]
	v_cvt_pk_bf16_f32 v36, v245, v249
	v_cvt_pk_bf16_f32 v37, v253, v191
	ds_write_b64 v200, v[36:37]
	s_waitcnt lgkmcnt(0)
	s_barrier
	s_nop 0
	v_mfma_f32_16x16x32_bf16 v[124:127], v[222:225], v[210:213], v[136:139]
	ds_read_b128 v[136:139], v177 offset:0
	ds_read_b128 v[140:143], v177 offset:0x2000
	v_mfma_f32_16x16x32_bf16 v[108:111], v[230:233], v[206:209], v[144:147]
	ds_read_b128 v[144:147], v177 offset:0x4000
	v_mfma_f32_16x16x32_bf16 v[104:107], v[226:229], v[206:209], v[148:151]
	ds_read_b128 v[148:151], v177 offset:0x6000
	v_mfma_f32_16x16x32_bf16 v[100:103], v[222:225], v[206:209], v[152:155]
	s_mov_b32 m0, s98
	s_add_i32 s15, s14, 0xffefff80
	buffer_load_dwordx4 v187, s[4:7], s15 offen lds
	ds_read_b128 v[152:155], v177 offset:0x8000
	ds_read_b128 v[156:159], v179 offset:0
	v_mfma_f32_16x16x32_bf16 v[96:99], v[230:233], v[202:205], v[160:163]
	ds_read_b128 v[160:163], v183 offset:0x800
	v_mfma_f32_16x16x32_bf16 v[84:87], v[222:225], v[202:205], v[168:171]
	v_mfma_f32_16x16x32_bf16 v[88:91], v[226:229], v[202:205], v[164:167]
	ds_read_b128 v[164:167], v179 offset:0x2000
	ds_read_b128 v[168:171], v183 offset:0x2800
	v_mfma_f32_16x16x32_bf16 v[92:95], v[234:237], v[202:205], v[92:95]
	s_add_i32 m0, s98, 0x2000
	s_add_i32 s64, s14, 0xfff3ff80
	buffer_load_dwordx4 v187, s[4:7], s64 offen lds
	v_mfma_f32_16x16x32_bf16 v[76:79], v[234:237], v[206:209], v[76:79]
	v_mfma_f32_16x16x32_bf16 v[132:135], v[226:229], v[210:213], v[132:135]
	v_mfma_f32_16x16x32_bf16 v[128:131], v[230:233], v[210:213], v[128:131]
	v_mfma_f32_16x16x32_bf16 v[64:67], v[234:237], v[210:213], v[64:67]
	s_add_i32 m0, s98, 0x4000
	s_add_i32 s15, s14, 0xfff7ff80
	buffer_load_dwordx4 v187, s[4:7], s15 offen lds
	v_mfma_f32_16x16x32_bf16 v[120:123], v[222:225], v[214:217], v[120:123]
	v_mfma_f32_16x16x32_bf16 v[116:119], v[226:229], v[214:217], v[116:119]
	v_mfma_f32_16x16x32_bf16 v[112:115], v[230:233], v[214:217], v[112:115]
	v_mfma_f32_16x16x32_bf16 v[60:63], v[234:237], v[214:217], v[60:63]
	s_add_i32 m0, s98, 0x6000
	s_add_i32 s64, s14, 0xfffbff80
	buffer_load_dwordx4 v187, s[4:7], s64 offen lds
	v_mfma_f32_16x16x32_bf16 v[68:71], v[222:225], v[218:221], v[68:71]
	v_mfma_f32_16x16x32_bf16 v[72:75], v[226:229], v[218:221], v[72:75]
	v_mfma_f32_16x16x32_bf16 v[80:83], v[230:233], v[218:221], v[80:83]
	v_mfma_f32_16x16x32_bf16 v[56:59], v[234:237], v[218:221], v[56:59]
	s_add_i32 m0, s98, 0x8000
	s_add_i32 s15, s14, 0xffffff80
	buffer_load_dwordx4 v187, s[4:7], s15 offen lds
	ds_read_b128 v[202:205], v181 offset:0
	ds_read_b128 v[206:209], v181 offset:0x2000
	ds_read_b128 v[210:213], v181 offset:0x4000
	ds_read_b128 v[214:217], v181 offset:0x6000
	ds_read_b128 v[218:221], v181 offset:0x8000
	ds_read_b128 v[222:225], v183 offset:0
	ds_read_b128 v[226:229], v179 offset:0x800
	ds_read_b128 v[230:233], v183 offset:0x2000
	ds_read_b128 v[234:237], v179 offset:0x2800
	s_waitcnt lgkmcnt(9)
	s_nop 0
	v_mfma_f32_16x16x32_bf16 v[84:87], v[156:159], v[136:139], v[84:87]
	v_mfma_f32_16x16x32_bf16 v[88:91], v[160:163], v[136:139], v[88:91]
	v_mfma_f32_16x16x32_bf16 v[96:99], v[164:167], v[136:139], v[96:99]
	v_mfma_f32_16x16x32_bf16 v[92:95], v[168:171], v[136:139], v[92:95]
	s_add_i32 s15, s3, 0xffffd000
	buffer_load_dwordx4 v[242:245], v173, s[8:11], s15 offen
	v_mfma_f32_16x16x32_bf16 v[100:103], v[156:159], v[140:143], v[100:103]
	v_mfma_f32_16x16x32_bf16 v[104:107], v[160:163], v[140:143], v[104:107]
	v_mfma_f32_16x16x32_bf16 v[108:111], v[164:167], v[140:143], v[108:111]
	v_mfma_f32_16x16x32_bf16 v[76:79], v[168:171], v[140:143], v[76:79]
	v_mfma_f32_16x16x32_bf16 v[124:127], v[156:159], v[144:147], v[124:127]
	s_add_i32 s64, s3, 0xffffe000
	buffer_load_dwordx4 v[246:249], v173, s[8:11], s64 offen
	v_mfma_f32_16x16x32_bf16 v[132:135], v[160:163], v[144:147], v[132:135]
	v_mfma_f32_16x16x32_bf16 v[128:131], v[164:167], v[144:147], v[128:131]
	v_mfma_f32_16x16x32_bf16 v[64:67], v[168:171], v[144:147], v[64:67]
	v_mfma_f32_16x16x32_bf16 v[120:123], v[156:159], v[148:151], v[120:123]
	v_mfma_f32_16x16x32_bf16 v[116:119], v[160:163], v[148:151], v[116:119]
	s_add_i32 s15, s3, 0xfffff000
	buffer_load_dwordx4 v[250:253], v173, s[8:11], s15 offen
	v_mfma_f32_16x16x32_bf16 v[112:115], v[164:167], v[148:151], v[112:115]
	v_mfma_f32_16x16x32_bf16 v[60:63], v[168:171], v[148:151], v[60:63]
	v_mfma_f32_16x16x32_bf16 v[68:71], v[156:159], v[152:155], v[68:71]
	v_mfma_f32_16x16x32_bf16 v[72:75], v[160:163], v[152:155], v[72:75]
	v_mfma_f32_16x16x32_bf16 v[80:83], v[164:167], v[152:155], v[80:83]
	buffer_load_dwordx4 v[188:191], v173, s[8:11], s3 offen
	v_mfma_f32_16x16x32_bf16 v[238:241], v[168:171], v[152:155], v[56:59]
	s_waitcnt vmcnt(4)
	v_cvt_pk_bf16_f32 v36, v24, v32
	v_cvt_pk_bf16_f32 v37, v20, v28
	ds_write_b64 v3, v[36:37] offset:49152
	v_cvt_pk_bf16_f32 v36, v25, v33
	v_cvt_pk_bf16_f32 v37, v21, v29
	ds_write_b64 v194, v[36:37] offset:49280
	v_cvt_pk_bf16_f32 v36, v26, v34
	v_cvt_pk_bf16_f32 v37, v22, v30
	ds_write_b64 v195, v[36:37] offset:49408
	v_cvt_pk_bf16_f32 v36, v27, v35
	v_cvt_pk_bf16_f32 v37, v23, v31
	ds_write_b64 v196, v[36:37] offset:49536
	s_waitcnt lgkmcnt(0)
	s_barrier
	s_nop 0
	v_mfma_f32_16x16x32_bf16 v[156:159], v[234:237], v[202:205], v[92:95]
	ds_read_b128 v[92:95], v176 offset:0
	v_mfma_f32_16x16x32_bf16 v[140:143], v[234:237], v[206:209], v[76:79]
	ds_read_b128 v[76:79], v176 offset:0x2000
	v_mfma_f32_16x16x32_bf16 v[136:139], v[222:225], v[210:213], v[124:127]
	v_mfma_f32_16x16x32_bf16 v[124:127], v[234:237], v[210:213], v[64:67]
	s_mov_b32 m0, s99
	s_add_i32 s15, s14, 0xfff00000
	buffer_load_dwordx4 v187, s[4:7], s15 offen lds
	ds_read_b128 v[64:67], v176 offset:0x4000
	v_mfma_f32_16x16x32_bf16 v[144:147], v[230:233], v[206:209], v[108:111]
	v_mfma_f32_16x16x32_bf16 v[108:111], v[234:237], v[214:217], v[60:63]
	ds_read_b128 v[60:63], v176 offset:0x6000
	ds_read_b128 v[56:59], v176 offset:0x8000
	v_mfma_f32_16x16x32_bf16 v[148:151], v[226:229], v[206:209], v[104:107]
	v_mfma_f32_16x16x32_bf16 v[104:107], v[222:225], v[218:221], v[68:71]
	s_add_i32 m0, s99, 0x2000
	s_add_i32 s64, s14, 0xfff40000
	buffer_load_dwordx4 v187, s[4:7], s64 offen lds
	ds_read_b128 v[68:71], v178 offset:0
	v_mfma_f32_16x16x32_bf16 v[152:155], v[222:225], v[206:209], v[100:103]
	v_mfma_f32_16x16x32_bf16 v[100:103], v[226:229], v[218:221], v[72:75]
	ds_read_b128 v[72:75], v182 offset:0x800
	v_mfma_f32_16x16x32_bf16 v[168:171], v[222:225], v[202:205], v[84:87]
	v_mfma_f32_16x16x32_bf16 v[164:167], v[226:229], v[202:205], v[88:91]
	s_add_i32 m0, s99, 0x4000
	s_add_i32 s15, s14, 0xfff80000
	buffer_load_dwordx4 v187, s[4:7], s15 offen lds
	v_mfma_f32_16x16x32_bf16 v[160:163], v[230:233], v[202:205], v[96:99]
	v_mfma_f32_16x16x32_bf16 v[132:135], v[226:229], v[210:213], v[132:135]
	v_mfma_f32_16x16x32_bf16 v[128:131], v[230:233], v[210:213], v[128:131]
	v_mfma_f32_16x16x32_bf16 v[120:123], v[222:225], v[214:217], v[120:123]
	s_add_i32 m0, s99, 0x6000
	s_add_i32 s64, s14, 0xfffc0000
	buffer_load_dwordx4 v187, s[4:7], s64 offen lds
	v_mfma_f32_16x16x32_bf16 v[116:119], v[226:229], v[214:217], v[116:119]
	v_mfma_f32_16x16x32_bf16 v[112:115], v[230:233], v[214:217], v[112:115]
	v_mfma_f32_16x16x32_bf16 v[96:99], v[230:233], v[218:221], v[80:83]
	ds_read_b128 v[80:83], v178 offset:0x2000
	ds_read_b128 v[84:87], v182 offset:0x2800
	v_mfma_f32_16x16x32_bf16 v[88:91], v[234:237], v[218:221], v[238:241]
	s_add_i32 m0, s99, 0x8000
	s_nop 0
	buffer_load_dwordx4 v187, s[4:7], s14 offen lds
	s_add_i32 s2, s2, 2
	s_add_i32 s3, s3, 0x80000
	s_addk_i32 s14, 0x100
	s_cmp_lt_u32 s2, 27
	s_cbranch_scc1 .LBB0_1327
	ds_read_b128 v[202:205], v180 offset:0
	ds_read_b128 v[206:209], v180 offset:0x2000
	ds_read_b128 v[210:213], v180 offset:0x4000
	ds_read_b128 v[214:217], v180 offset:0x6000
	ds_read_b128 v[218:221], v180 offset:0x8000
	ds_read_b128 v[222:225], v182 offset:0
	ds_read_b128 v[226:229], v178 offset:0x800
	ds_read_b128 v[230:233], v182 offset:0x2000
	ds_read_b128 v[234:237], v178 offset:0x2800
	s_waitcnt lgkmcnt(9)
	s_nop 0
	v_mfma_f32_16x16x32_bf16 v[168:171], v[68:71], v[92:95], v[168:171]
	v_mfma_f32_16x16x32_bf16 v[164:167], v[72:75], v[92:95], v[164:167]
	v_mfma_f32_16x16x32_bf16 v[160:163], v[80:83], v[92:95], v[160:163]
	v_mfma_f32_16x16x32_bf16 v[92:95], v[84:87], v[92:95], v[156:159]
	v_mfma_f32_16x16x32_bf16 v[152:155], v[68:71], v[76:79], v[152:155]
	v_mfma_f32_16x16x32_bf16 v[148:151], v[72:75], v[76:79], v[148:151]
	v_mfma_f32_16x16x32_bf16 v[144:147], v[80:83], v[76:79], v[144:147]
	v_mfma_f32_16x16x32_bf16 v[76:79], v[84:87], v[76:79], v[140:143]
	v_mfma_f32_16x16x32_bf16 v[136:139], v[68:71], v[64:67], v[136:139]
	v_mfma_f32_16x16x32_bf16 v[132:135], v[72:75], v[64:67], v[132:135]
	v_mfma_f32_16x16x32_bf16 v[128:131], v[80:83], v[64:67], v[128:131]
	v_mfma_f32_16x16x32_bf16 v[124:127], v[84:87], v[64:67], v[124:127]
	v_mfma_f32_16x16x32_bf16 v[120:123], v[68:71], v[60:63], v[120:123]
	v_mfma_f32_16x16x32_bf16 v[116:119], v[72:75], v[60:63], v[116:119]
	v_mfma_f32_16x16x32_bf16 v[112:115], v[80:83], v[60:63], v[112:115]
	v_mfma_f32_16x16x32_bf16 v[108:111], v[84:87], v[60:63], v[108:111]
	v_mfma_f32_16x16x32_bf16 v[104:107], v[68:71], v[56:59], v[104:107]
	v_mfma_f32_16x16x32_bf16 v[140:143], v[72:75], v[56:59], v[100:103]
	v_mfma_f32_16x16x32_bf16 v[156:159], v[80:83], v[56:59], v[96:99]
	v_mfma_f32_16x16x32_bf16 v[238:241], v[84:87], v[56:59], v[88:91]
	s_waitcnt vmcnt(0)
	v_cvt_pk_bf16_f32 v36, v242, v246
	v_cvt_pk_bf16_f32 v37, v250, v188
	ds_write_b64 v197, v[36:37]
	v_cvt_pk_bf16_f32 v36, v243, v247
	v_cvt_pk_bf16_f32 v37, v251, v189
	ds_write_b64 v198, v[36:37]
	v_cvt_pk_bf16_f32 v36, v244, v248
	v_cvt_pk_bf16_f32 v37, v252, v190
	ds_write_b64 v199, v[36:37]
	v_cvt_pk_bf16_f32 v36, v245, v249
	v_cvt_pk_bf16_f32 v37, v253, v191
	ds_write_b64 v200, v[36:37]
	s_waitcnt lgkmcnt(0)
	s_barrier
	s_nop 0
	v_mfma_f32_16x16x32_bf16 v[56:59], v[226:229], v[206:209], v[148:151]
	ds_read_b128 v[148:151], v177 offset:0
	v_mfma_f32_16x16x32_bf16 v[60:63], v[230:233], v[206:209], v[144:147]
	ds_read_b128 v[144:147], v177 offset:0x2000
	v_mfma_f32_16x16x32_bf16 v[80:83], v[234:237], v[210:213], v[124:127]
	ds_read_b128 v[124:127], v177 offset:0x4000
	v_mfma_f32_16x16x32_bf16 v[88:91], v[226:229], v[214:217], v[116:119]
	ds_read_b128 v[116:119], v177 offset:0x6000
	v_mfma_f32_16x16x32_bf16 v[96:99], v[234:237], v[214:217], v[108:111]
	ds_read_b128 v[108:111], v177 offset:0x8000
	v_mfma_f32_16x16x32_bf16 v[84:87], v[222:225], v[214:217], v[120:123]
	ds_read_b128 v[120:123], v179 offset:0
	v_mfma_f32_16x16x32_bf16 v[64:67], v[234:237], v[206:209], v[76:79]
	v_mfma_f32_16x16x32_bf16 v[76:79], v[230:233], v[210:213], v[128:131]
	ds_read_b128 v[128:131], v183 offset:0x800
	v_mfma_f32_16x16x32_bf16 v[20:23], v[222:225], v[202:205], v[168:171]
	v_mfma_f32_16x16x32_bf16 v[24:27], v[226:229], v[202:205], v[164:167]
	v_mfma_f32_16x16x32_bf16 v[28:31], v[230:233], v[202:205], v[160:163]
	v_mfma_f32_16x16x32_bf16 v[32:35], v[234:237], v[202:205], v[92:95]
	v_mfma_f32_16x16x32_bf16 v[52:55], v[222:225], v[206:209], v[152:155]
	v_mfma_f32_16x16x32_bf16 v[68:71], v[222:225], v[210:213], v[136:139]
	v_mfma_f32_16x16x32_bf16 v[72:75], v[226:229], v[210:213], v[132:135]
	ds_read_b128 v[132:135], v179 offset:0x2000
	ds_read_b128 v[136:139], v183 offset:0x2800
	v_mfma_f32_16x16x32_bf16 v[92:95], v[230:233], v[214:217], v[112:115]
	v_mfma_f32_16x16x32_bf16 v[100:103], v[222:225], v[218:221], v[104:107]
	v_mfma_f32_16x16x32_bf16 v[104:107], v[226:229], v[218:221], v[140:143]
	v_mfma_f32_16x16x32_bf16 v[112:115], v[230:233], v[218:221], v[156:159]
	v_mfma_f32_16x16x32_bf16 v[140:143], v[234:237], v[218:221], v[238:241]
	s_add_i32 s2, s59, 0x140
	s_cmp_ge_i32 s2, s55
	s_cselect_b64 s[2:3], -1, 0
	s_and_b64 s[2:3], s[20:21], s[2:3]
	v_mov_b64_e32 v[50:51], v[6:7]
	v_mov_b64_e32 v[46:47], v[10:11]
	v_mov_b64_e32 v[42:43], v[14:15]
	v_mov_b64_e32 v[38:39], v[18:19]
	s_andn2_b64 vcc, exec, s[2:3]
	v_mov_b64_e32 v[48:49], v[4:5]
	v_mov_b64_e32 v[44:45], v[8:9]
	v_mov_b64_e32 v[40:41], v[12:13]
	v_mov_b64_e32 v[36:37], v[16:17]
	s_cbranch_vccnz .LBB0_1330
	s_mov_b32 s14, s10
	s_mov_b32 s15, s11
	buffer_load_dwordx4 v[48:51], v173, s[12:15], 0 offen
	buffer_load_dwordx4 v[44:47], v173, s[12:15], s44 offen
	buffer_load_dwordx4 v[40:43], v173, s[12:15], s45 offen
	buffer_load_dwordx4 v[36:39], v173, s[12:15], s46 offen

.LBB0_1340:
	ds_read_b128 v[148:151], v180 offset:0
	ds_read_b128 v[152:155], v180 offset:0x2000
	ds_read_b128 v[156:159], v180 offset:0x4000
	ds_read_b128 v[160:163], v180 offset:0x6000
	ds_read_b128 v[164:167], v182 offset:0
	ds_read_b128 v[168:171], v178 offset:0x800
	ds_read_b128 v[202:205], v182 offset:0x2000
	ds_read_b128 v[206:209], v178 offset:0x2800
	s_waitcnt lgkmcnt(8)
	s_nop 1
	v_mfma_f32_16x16x32_bf16 v[144:147], v[64:67], v[72:75], v[144:147]
	v_mfma_f32_16x16x32_bf16 v[140:143], v[68:71], v[72:75], v[140:143]
	v_mfma_f32_16x16x32_bf16 v[136:139], v[76:79], v[72:75], v[136:139]
	v_mfma_f32_16x16x32_bf16 v[72:75], v[80:83], v[72:75], v[132:135]
	s_add_i32 s15, s3, 0xfffbd000
	buffer_load_dwordx4 v[24:27], v173, s[8:11], s15 offen
	v_mfma_f32_16x16x32_bf16 v[128:131], v[64:67], v[60:63], v[128:131]
	v_mfma_f32_16x16x32_bf16 v[124:127], v[68:71], v[60:63], v[124:127]
	v_mfma_f32_16x16x32_bf16 v[120:123], v[76:79], v[60:63], v[120:123]
	v_mfma_f32_16x16x32_bf16 v[60:63], v[80:83], v[60:63], v[116:119]
	s_add_i32 s23, s3, 0xfffbe000
	buffer_load_dwordx4 v[32:35], v173, s[8:11], s23 offen
	v_mfma_f32_16x16x32_bf16 v[112:115], v[64:67], v[56:59], v[112:115]
	v_mfma_f32_16x16x32_bf16 v[108:111], v[68:71], v[56:59], v[108:111]
	v_mfma_f32_16x16x32_bf16 v[104:107], v[76:79], v[56:59], v[104:107]
	v_mfma_f32_16x16x32_bf16 v[56:59], v[80:83], v[56:59], v[100:103]
	s_add_i32 s15, s3, 0xfffbf000
	buffer_load_dwordx4 v[20:23], v173, s[8:11], s15 offen
	v_mfma_f32_16x16x32_bf16 v[64:67], v[64:67], v[52:55], v[96:99]
	v_mfma_f32_16x16x32_bf16 v[68:71], v[68:71], v[52:55], v[92:95]
	v_mfma_f32_16x16x32_bf16 v[76:79], v[76:79], v[52:55], v[88:91]
	v_mfma_f32_16x16x32_bf16 v[52:55], v[80:83], v[52:55], v[84:87]
	s_add_i32 s23, s3, 0xfffc0000
	buffer_load_dwordx4 v[28:31], v173, s[8:11], s23 offen
	s_waitcnt vmcnt(4)
	v_cvt_pk_bf16_f32 v36, v242, v246
	v_cvt_pk_bf16_f32 v37, v250, v188
	ds_write_b64 v197, v[36:37]
	v_cvt_pk_bf16_f32 v36, v243, v247
	v_cvt_pk_bf16_f32 v37, v251, v189
	ds_write_b64 v198, v[36:37]
	v_cvt_pk_bf16_f32 v36, v244, v248
	v_cvt_pk_bf16_f32 v37, v252, v190
	ds_write_b64 v199, v[36:37]
	v_cvt_pk_bf16_f32 v36, v245, v249
	v_cvt_pk_bf16_f32 v37, v253, v191
	ds_write_b64 v200, v[36:37]
	s_waitcnt lgkmcnt(0)
	s_barrier
	ds_read_b128 v[116:119], v177 offset:0
	s_nop 0
	v_mfma_f32_16x16x32_bf16 v[100:103], v[202:205], v[152:155], v[120:123]
	ds_read_b128 v[120:123], v177 offset:0x2000
	v_mfma_f32_16x16x32_bf16 v[96:99], v[168:171], v[152:155], v[124:127]
	ds_read_b128 v[124:127], v177 offset:0x4000
	v_mfma_f32_16x16x32_bf16 v[92:95], v[164:167], v[152:155], v[128:131]
	ds_read_b128 v[128:131], v177 offset:0x6000
	ds_read_b128 v[132:135], v179 offset:0
	v_mfma_f32_16x16x32_bf16 v[88:91], v[202:205], v[148:151], v[136:139]
	s_mov_b32 m0, s98
	s_add_i32 s15, s14, 0xfff3ff80
	buffer_load_dwordx4 v187, s[4:7], s15 offen lds
	ds_read_b128 v[136:139], v183 offset:0x800
	v_mfma_f32_16x16x32_bf16 v[80:83], v[164:167], v[148:151], v[144:147]
	v_mfma_f32_16x16x32_bf16 v[84:87], v[168:171], v[148:151], v[140:143]
	ds_read_b128 v[140:143], v179 offset:0x2000
	ds_read_b128 v[144:147], v183 offset:0x2800
	v_mfma_f32_16x16x32_bf16 v[72:75], v[206:209], v[148:151], v[72:75]
	v_mfma_f32_16x16x32_bf16 v[60:63], v[206:209], v[152:155], v[60:63]
	s_add_i32 m0, s98, 0x2000
	s_add_i32 s23, s14, 0xfff7ff80
	buffer_load_dwordx4 v187, s[4:7], s23 offen lds
	v_mfma_f32_16x16x32_bf16 v[112:115], v[164:167], v[156:159], v[112:115]
	v_mfma_f32_16x16x32_bf16 v[108:111], v[168:171], v[156:159], v[108:111]
	v_mfma_f32_16x16x32_bf16 v[104:107], v[202:205], v[156:159], v[104:107]
	v_mfma_f32_16x16x32_bf16 v[56:59], v[206:209], v[156:159], v[56:59]
	s_add_i32 m0, s98, 0x4000
	s_add_i32 s15, s14, 0xfffbff80
	buffer_load_dwordx4 v187, s[4:7], s15 offen lds
	v_mfma_f32_16x16x32_bf16 v[64:67], v[164:167], v[160:163], v[64:67]
	v_mfma_f32_16x16x32_bf16 v[68:71], v[168:171], v[160:163], v[68:71]
	v_mfma_f32_16x16x32_bf16 v[76:79], v[202:205], v[160:163], v[76:79]
	v_mfma_f32_16x16x32_bf16 v[52:55], v[206:209], v[160:163], v[52:55]
	s_add_i32 m0, s98, 0x6000
	s_add_i32 s23, s14, 0xffffff80
	buffer_load_dwordx4 v187, s[4:7], s23 offen lds
	ds_read_b128 v[148:151], v181 offset:0
	ds_read_b128 v[152:155], v181 offset:0x2000
	ds_read_b128 v[156:159], v181 offset:0x4000
	ds_read_b128 v[160:163], v181 offset:0x6000
	ds_read_b128 v[164:167], v183 offset:0
	ds_read_b128 v[168:171], v179 offset:0x800
	ds_read_b128 v[202:205], v183 offset:0x2000
	ds_read_b128 v[206:209], v179 offset:0x2800
	s_waitcnt lgkmcnt(8)
	s_nop 0
	v_mfma_f32_16x16x32_bf16 v[80:83], v[132:135], v[116:119], v[80:83]
	v_mfma_f32_16x16x32_bf16 v[84:87], v[136:139], v[116:119], v[84:87]
	v_mfma_f32_16x16x32_bf16 v[88:91], v[140:143], v[116:119], v[88:91]
	v_mfma_f32_16x16x32_bf16 v[72:75], v[144:147], v[116:119], v[72:75]
	s_add_i32 s15, s3, 0xffffd000
	buffer_load_dwordx4 v[242:245], v173, s[8:11], s15 offen
	v_mfma_f32_16x16x32_bf16 v[92:95], v[132:135], v[120:123], v[92:95]
	v_mfma_f32_16x16x32_bf16 v[96:99], v[136:139], v[120:123], v[96:99]
	v_mfma_f32_16x16x32_bf16 v[100:103], v[140:143], v[120:123], v[100:103]
	v_mfma_f32_16x16x32_bf16 v[60:63], v[144:147], v[120:123], v[60:63]
	s_add_i32 s23, s3, 0xffffe000
	buffer_load_dwordx4 v[246:249], v173, s[8:11], s23 offen
	v_mfma_f32_16x16x32_bf16 v[112:115], v[132:135], v[124:127], v[112:115]
	v_mfma_f32_16x16x32_bf16 v[108:111], v[136:139], v[124:127], v[108:111]
	v_mfma_f32_16x16x32_bf16 v[104:107], v[140:143], v[124:127], v[104:107]
	v_mfma_f32_16x16x32_bf16 v[56:59], v[144:147], v[124:127], v[56:59]
	s_add_i32 s15, s3, 0xfffff000
	buffer_load_dwordx4 v[250:253], v173, s[8:11], s15 offen
	v_mfma_f32_16x16x32_bf16 v[64:67], v[132:135], v[128:131], v[64:67]
	v_mfma_f32_16x16x32_bf16 v[68:71], v[136:139], v[128:131], v[68:71]
	v_mfma_f32_16x16x32_bf16 v[76:79], v[140:143], v[128:131], v[76:79]
	v_mfma_f32_16x16x32_bf16 v[210:213], v[144:147], v[128:131], v[52:55]
	buffer_load_dwordx4 v[188:191], v173, s[8:11], s3 offen
	s_waitcnt vmcnt(4)
	v_cvt_pk_bf16_f32 v36, v24, v32
	v_cvt_pk_bf16_f32 v37, v20, v28
	ds_write_b64 v3, v[36:37] offset:49152
	v_cvt_pk_bf16_f32 v36, v25, v33
	v_cvt_pk_bf16_f32 v37, v21, v29
	ds_write_b64 v194, v[36:37] offset:49280
	v_cvt_pk_bf16_f32 v36, v26, v34
	v_cvt_pk_bf16_f32 v37, v22, v30
	ds_write_b64 v195, v[36:37] offset:49408
	v_cvt_pk_bf16_f32 v36, v27, v35
	v_cvt_pk_bf16_f32 v37, v23, v31
	ds_write_b64 v196, v[36:37] offset:49536
	s_waitcnt lgkmcnt(0)
	s_barrier
	s_nop 0
	v_mfma_f32_16x16x32_bf16 v[132:135], v[206:209], v[148:151], v[72:75]
	ds_read_b128 v[72:75], v176 offset:0
	v_mfma_f32_16x16x32_bf16 v[116:119], v[206:209], v[152:155], v[60:63]
	ds_read_b128 v[60:63], v176 offset:0x2000
	v_mfma_f32_16x16x32_bf16 v[120:123], v[202:205], v[152:155], v[100:103]
	v_mfma_f32_16x16x32_bf16 v[100:103], v[206:209], v[156:159], v[56:59]
	s_mov_b32 m0, s99
	s_add_i32 s15, s14, 0xfff40000
	buffer_load_dwordx4 v187, s[4:7], s15 offen lds
	ds_read_b128 v[56:59], v176 offset:0x4000
	ds_read_b128 v[52:55], v176 offset:0x6000
	v_mfma_f32_16x16x32_bf16 v[124:127], v[168:171], v[152:155], v[96:99]
	v_mfma_f32_16x16x32_bf16 v[96:99], v[164:167], v[160:163], v[64:67]
	ds_read_b128 v[64:67], v178 offset:0
	v_mfma_f32_16x16x32_bf16 v[128:131], v[164:167], v[152:155], v[92:95]
	v_mfma_f32_16x16x32_bf16 v[92:95], v[168:171], v[160:163], v[68:71]
	s_add_i32 m0, s99, 0x2000
	s_add_i32 s23, s14, 0xfff80000
	buffer_load_dwordx4 v187, s[4:7], s23 offen lds
	ds_read_b128 v[68:71], v182 offset:0x800
	v_mfma_f32_16x16x32_bf16 v[144:147], v[164:167], v[148:151], v[80:83]
	v_mfma_f32_16x16x32_bf16 v[140:143], v[168:171], v[148:151], v[84:87]
	v_mfma_f32_16x16x32_bf16 v[136:139], v[202:205], v[148:151], v[88:91]
	v_mfma_f32_16x16x32_bf16 v[112:115], v[164:167], v[156:159], v[112:115]
	s_add_i32 m0, s99, 0x4000
	s_add_i32 s15, s14, 0xfffc0000
	buffer_load_dwordx4 v187, s[4:7], s15 offen lds
	v_mfma_f32_16x16x32_bf16 v[108:111], v[168:171], v[156:159], v[108:111]
	v_mfma_f32_16x16x32_bf16 v[104:107], v[202:205], v[156:159], v[104:107]
	v_mfma_f32_16x16x32_bf16 v[88:91], v[202:205], v[160:163], v[76:79]
	ds_read_b128 v[76:79], v178 offset:0x2000
	ds_read_b128 v[80:83], v182 offset:0x2800
	v_mfma_f32_16x16x32_bf16 v[84:87], v[206:209], v[160:163], v[210:213]
	s_add_i32 m0, s99, 0x6000
	s_nop 0
	buffer_load_dwordx4 v187, s[4:7], s14 offen lds
	s_add_i32 s2, s2, 2
	s_add_i32 s3, s3, 0x80000
	s_addk_i32 s14, 0x100
	s_cmp_lt_u32 s2, 27
	s_cbranch_scc1 .LBB0_1340
	ds_read_b128 v[148:151], v180 offset:0
	ds_read_b128 v[152:155], v180 offset:0x2000
	ds_read_b128 v[156:159], v180 offset:0x4000
	ds_read_b128 v[160:163], v180 offset:0x6000
	ds_read_b128 v[164:167], v182 offset:0
	ds_read_b128 v[168:171], v178 offset:0x800
	ds_read_b128 v[202:205], v182 offset:0x2000
	ds_read_b128 v[206:209], v178 offset:0x2800
	s_waitcnt lgkmcnt(8)
	s_nop 0
	v_mfma_f32_16x16x32_bf16 v[144:147], v[64:67], v[72:75], v[144:147]
	v_mfma_f32_16x16x32_bf16 v[140:143], v[68:71], v[72:75], v[140:143]
	v_mfma_f32_16x16x32_bf16 v[136:139], v[76:79], v[72:75], v[136:139]
	v_mfma_f32_16x16x32_bf16 v[72:75], v[80:83], v[72:75], v[132:135]
	v_mfma_f32_16x16x32_bf16 v[128:131], v[64:67], v[60:63], v[128:131]
	v_mfma_f32_16x16x32_bf16 v[124:127], v[68:71], v[60:63], v[124:127]
	v_mfma_f32_16x16x32_bf16 v[120:123], v[76:79], v[60:63], v[120:123]
	v_mfma_f32_16x16x32_bf16 v[60:63], v[80:83], v[60:63], v[116:119]
	v_mfma_f32_16x16x32_bf16 v[112:115], v[64:67], v[56:59], v[112:115]
	v_mfma_f32_16x16x32_bf16 v[108:111], v[68:71], v[56:59], v[108:111]
	v_mfma_f32_16x16x32_bf16 v[104:107], v[76:79], v[56:59], v[104:107]
	v_mfma_f32_16x16x32_bf16 v[100:103], v[80:83], v[56:59], v[100:103]
	v_mfma_f32_16x16x32_bf16 v[96:99], v[64:67], v[52:55], v[96:99]
	v_mfma_f32_16x16x32_bf16 v[116:119], v[68:71], v[52:55], v[92:95]
	v_mfma_f32_16x16x32_bf16 v[132:135], v[76:79], v[52:55], v[88:91]
	v_mfma_f32_16x16x32_bf16 v[210:213], v[80:83], v[52:55], v[84:87]
	s_waitcnt vmcnt(0)
	v_cvt_pk_bf16_f32 v36, v242, v246
	v_cvt_pk_bf16_f32 v37, v250, v188
	ds_write_b64 v197, v[36:37]
	v_cvt_pk_bf16_f32 v36, v243, v247
	v_cvt_pk_bf16_f32 v37, v251, v189
	ds_write_b64 v198, v[36:37]
	v_cvt_pk_bf16_f32 v36, v244, v248
	v_cvt_pk_bf16_f32 v37, v252, v190
	ds_write_b64 v199, v[36:37]
	v_cvt_pk_bf16_f32 v36, v245, v249
	v_cvt_pk_bf16_f32 v37, v253, v191
	ds_write_b64 v200, v[36:37]
	s_waitcnt lgkmcnt(0)
	s_barrier
	s_nop 0
	v_mfma_f32_16x16x32_bf16 v[52:55], v[164:167], v[156:159], v[112:115]
	ds_read_b128 v[112:115], v177 offset:0
	ds_read_b128 v[92:95], v177 offset:0x2000
	ds_read_b128 v[84:87], v177 offset:0x4000
	ds_read_b128 v[76:79], v177 offset:0x6000
	ds_read_b128 v[88:91], v179 offset:0
	v_mfma_f32_16x16x32_bf16 v[68:71], v[164:167], v[160:163], v[96:99]
	ds_read_b128 v[96:99], v183 offset:0x800
	v_mfma_f32_16x16x32_bf16 v[20:23], v[164:167], v[148:151], v[144:147]
	v_mfma_f32_16x16x32_bf16 v[24:27], v[168:171], v[148:151], v[140:143]
	v_mfma_f32_16x16x32_bf16 v[28:31], v[202:205], v[148:151], v[136:139]
	v_mfma_f32_16x16x32_bf16 v[32:35], v[206:209], v[148:151], v[72:75]
	v_mfma_f32_16x16x32_bf16 v[36:39], v[164:167], v[152:155], v[128:131]
	v_mfma_f32_16x16x32_bf16 v[40:43], v[168:171], v[152:155], v[124:127]
	v_mfma_f32_16x16x32_bf16 v[44:47], v[202:205], v[152:155], v[120:123]
	v_mfma_f32_16x16x32_bf16 v[48:51], v[206:209], v[152:155], v[60:63]
	v_mfma_f32_16x16x32_bf16 v[56:59], v[168:171], v[156:159], v[108:111]
	v_mfma_f32_16x16x32_bf16 v[60:63], v[202:205], v[156:159], v[104:107]
	v_mfma_f32_16x16x32_bf16 v[64:67], v[206:209], v[156:159], v[100:103]
	ds_read_b128 v[100:103], v179 offset:0x2000
	ds_read_b128 v[104:107], v183 offset:0x2800
	v_mfma_f32_16x16x32_bf16 v[72:75], v[168:171], v[160:163], v[116:119]
	v_mfma_f32_16x16x32_bf16 v[80:83], v[202:205], v[160:163], v[132:135]
	v_mfma_f32_16x16x32_bf16 v[108:111], v[206:209], v[160:163], v[210:213]
	s_andn2_b64 vcc, exec, s[20:21]
	s_cbranch_vccnz .LBB0_1343
	s_mov_b32 s14, s10
	s_mov_b32 s15, s11
	buffer_load_dwordx4 v[4:7], v173, s[12:15], 0 offen
	buffer_load_dwordx4 v[8:11], v173, s[12:15], s44 offen
	buffer_load_dwordx4 v[12:15], v173, s[12:15], s45 offen
	buffer_load_dwordx4 v[16:19], v173, s[12:15], s46 offen

.LBB0_1430:
	ds_read_b128 v[202:205], v180 offset:0
	ds_read_b128 v[206:209], v180 offset:0x2000
	ds_read_b128 v[210:213], v180 offset:0x4000
	ds_read_b128 v[214:217], v180 offset:0x6000
	ds_read_b128 v[218:221], v180 offset:0x8000
	ds_read_b128 v[222:225], v182 offset:0
	ds_read_b128 v[226:229], v178 offset:0x800
	ds_read_b128 v[230:233], v182 offset:0x1000
	ds_read_b128 v[234:237], v178 offset:0x1800
	s_waitcnt lgkmcnt(9)
	s_nop 1
	v_mfma_f32_16x16x32_bf16 v[168:171], v[68:71], v[92:95], v[168:171]
	v_mfma_f32_16x16x32_bf16 v[164:167], v[72:75], v[92:95], v[164:167]
	v_mfma_f32_16x16x32_bf16 v[160:163], v[80:83], v[92:95], v[160:163]
	v_mfma_f32_16x16x32_bf16 v[92:95], v[84:87], v[92:95], v[156:159]
	s_add_i32 s15, s3, 0xfff7a000
	buffer_load_dwordx4 v[24:27], v173, s[8:11], s15 offen
	v_mfma_f32_16x16x32_bf16 v[152:155], v[68:71], v[76:79], v[152:155]
	v_mfma_f32_16x16x32_bf16 v[148:151], v[72:75], v[76:79], v[148:151]
	v_mfma_f32_16x16x32_bf16 v[144:147], v[80:83], v[76:79], v[144:147]
	v_mfma_f32_16x16x32_bf16 v[76:79], v[84:87], v[76:79], v[140:143]
	v_mfma_f32_16x16x32_bf16 v[136:139], v[68:71], v[64:67], v[136:139]
	s_add_i32 s65, s3, 0xfff7c000
	buffer_load_dwordx4 v[32:35], v173, s[8:11], s65 offen
	v_mfma_f32_16x16x32_bf16 v[132:135], v[72:75], v[64:67], v[132:135]
	v_mfma_f32_16x16x32_bf16 v[128:131], v[80:83], v[64:67], v[128:131]
	v_mfma_f32_16x16x32_bf16 v[64:67], v[84:87], v[64:67], v[124:127]
	v_mfma_f32_16x16x32_bf16 v[120:123], v[68:71], v[60:63], v[120:123]
	v_mfma_f32_16x16x32_bf16 v[116:119], v[72:75], v[60:63], v[116:119]
	s_add_i32 s15, s3, 0xfff7e000
	buffer_load_dwordx4 v[20:23], v173, s[8:11], s15 offen
	v_mfma_f32_16x16x32_bf16 v[112:115], v[80:83], v[60:63], v[112:115]
	v_mfma_f32_16x16x32_bf16 v[60:63], v[84:87], v[60:63], v[108:111]
	v_mfma_f32_16x16x32_bf16 v[68:71], v[68:71], v[56:59], v[104:107]
	v_mfma_f32_16x16x32_bf16 v[72:75], v[72:75], v[56:59], v[100:103]
	v_mfma_f32_16x16x32_bf16 v[80:83], v[80:83], v[56:59], v[96:99]
	s_add_i32 s65, s3, 0xfff80000
	buffer_load_dwordx4 v[28:31], v173, s[8:11], s65 offen
	v_mfma_f32_16x16x32_bf16 v[56:59], v[84:87], v[56:59], v[88:91]
	s_waitcnt vmcnt(4)
	v_cvt_pk_bf16_f32 v36, v242, v246
	v_cvt_pk_bf16_f32 v37, v250, v188
	ds_write_b64 v197, v[36:37]
	v_cvt_pk_bf16_f32 v36, v243, v247
	v_cvt_pk_bf16_f32 v37, v251, v189
	ds_write_b64 v198, v[36:37]
	v_cvt_pk_bf16_f32 v36, v244, v248
	v_cvt_pk_bf16_f32 v37, v252, v190
	ds_write_b64 v199, v[36:37]
	v_cvt_pk_bf16_f32 v36, v245, v249
	v_cvt_pk_bf16_f32 v37, v253, v191
	ds_write_b64 v200, v[36:37]
	s_waitcnt lgkmcnt(0)
	s_barrier
	s_nop 0
	v_mfma_f32_16x16x32_bf16 v[124:127], v[222:225], v[210:213], v[136:139]
	ds_read_b128 v[136:139], v177 offset:0
	ds_read_b128 v[140:143], v177 offset:0x2000
	v_mfma_f32_16x16x32_bf16 v[108:111], v[230:233], v[206:209], v[144:147]
	ds_read_b128 v[144:147], v177 offset:0x4000
	v_mfma_f32_16x16x32_bf16 v[104:107], v[226:229], v[206:209], v[148:151]
	ds_read_b128 v[148:151], v177 offset:0x6000
	v_mfma_f32_16x16x32_bf16 v[100:103], v[222:225], v[206:209], v[152:155]
	s_mov_b32 m0, s98
	s_add_i32 s15, s14, 0xfff7ff80
	buffer_load_dwordx4 v187, s[4:7], s15 offen lds
	ds_read_b128 v[152:155], v177 offset:0x8000
	ds_read_b128 v[156:159], v179 offset:0
	v_mfma_f32_16x16x32_bf16 v[96:99], v[230:233], v[202:205], v[160:163]
	ds_read_b128 v[160:163], v183 offset:0x800
	v_mfma_f32_16x16x32_bf16 v[84:87], v[222:225], v[202:205], v[168:171]
	v_mfma_f32_16x16x32_bf16 v[88:91], v[226:229], v[202:205], v[164:167]
	ds_read_b128 v[164:167], v179 offset:0x1000
	ds_read_b128 v[168:171], v183 offset:0x1800
	v_mfma_f32_16x16x32_bf16 v[92:95], v[234:237], v[202:205], v[92:95]
	s_add_i32 m0, s98, 0x2000
	s_add_i32 s65, s14, 0xfff9ff80
	buffer_load_dwordx4 v187, s[4:7], s65 offen lds
	v_mfma_f32_16x16x32_bf16 v[76:79], v[234:237], v[206:209], v[76:79]
	v_mfma_f32_16x16x32_bf16 v[132:135], v[226:229], v[210:213], v[132:135]
	v_mfma_f32_16x16x32_bf16 v[128:131], v[230:233], v[210:213], v[128:131]
	v_mfma_f32_16x16x32_bf16 v[64:67], v[234:237], v[210:213], v[64:67]
	s_add_i32 m0, s98, 0x4000
	s_add_i32 s15, s14, 0xfffbff80
	buffer_load_dwordx4 v187, s[4:7], s15 offen lds
	v_mfma_f32_16x16x32_bf16 v[120:123], v[222:225], v[214:217], v[120:123]
	v_mfma_f32_16x16x32_bf16 v[116:119], v[226:229], v[214:217], v[116:119]
	v_mfma_f32_16x16x32_bf16 v[112:115], v[230:233], v[214:217], v[112:115]
	v_mfma_f32_16x16x32_bf16 v[60:63], v[234:237], v[214:217], v[60:63]
	s_add_i32 m0, s98, 0x6000
	s_add_i32 s65, s14, 0xfffdff80
	buffer_load_dwordx4 v187, s[4:7], s65 offen lds
	v_mfma_f32_16x16x32_bf16 v[68:71], v[222:225], v[218:221], v[68:71]
	v_mfma_f32_16x16x32_bf16 v[72:75], v[226:229], v[218:221], v[72:75]
	v_mfma_f32_16x16x32_bf16 v[80:83], v[230:233], v[218:221], v[80:83]
	v_mfma_f32_16x16x32_bf16 v[56:59], v[234:237], v[218:221], v[56:59]
	s_add_i32 m0, s98, 0x8000
	s_add_i32 s15, s14, 0xffffff80
	buffer_load_dwordx4 v187, s[4:7], s15 offen lds
	ds_read_b128 v[202:205], v181 offset:0
	ds_read_b128 v[206:209], v181 offset:0x2000
	ds_read_b128 v[210:213], v181 offset:0x4000
	ds_read_b128 v[214:217], v181 offset:0x6000
	ds_read_b128 v[218:221], v181 offset:0x8000
	ds_read_b128 v[222:225], v183 offset:0
	ds_read_b128 v[226:229], v179 offset:0x800
	ds_read_b128 v[230:233], v183 offset:0x1000
	ds_read_b128 v[234:237], v179 offset:0x1800
	s_waitcnt lgkmcnt(9)
	s_nop 0
	v_mfma_f32_16x16x32_bf16 v[84:87], v[156:159], v[136:139], v[84:87]
	v_mfma_f32_16x16x32_bf16 v[88:91], v[160:163], v[136:139], v[88:91]
	v_mfma_f32_16x16x32_bf16 v[96:99], v[164:167], v[136:139], v[96:99]
	v_mfma_f32_16x16x32_bf16 v[92:95], v[168:171], v[136:139], v[92:95]
	s_add_i32 s15, s3, 0xffffa000
	buffer_load_dwordx4 v[242:245], v173, s[8:11], s15 offen
	v_mfma_f32_16x16x32_bf16 v[100:103], v[156:159], v[140:143], v[100:103]
	v_mfma_f32_16x16x32_bf16 v[104:107], v[160:163], v[140:143], v[104:107]
	v_mfma_f32_16x16x32_bf16 v[108:111], v[164:167], v[140:143], v[108:111]
	v_mfma_f32_16x16x32_bf16 v[76:79], v[168:171], v[140:143], v[76:79]
	v_mfma_f32_16x16x32_bf16 v[124:127], v[156:159], v[144:147], v[124:127]
	s_add_i32 s65, s3, 0xffffc000
	buffer_load_dwordx4 v[246:249], v173, s[8:11], s65 offen
	v_mfma_f32_16x16x32_bf16 v[132:135], v[160:163], v[144:147], v[132:135]
	v_mfma_f32_16x16x32_bf16 v[128:131], v[164:167], v[144:147], v[128:131]
	v_mfma_f32_16x16x32_bf16 v[64:67], v[168:171], v[144:147], v[64:67]
	v_mfma_f32_16x16x32_bf16 v[120:123], v[156:159], v[148:151], v[120:123]
	v_mfma_f32_16x16x32_bf16 v[116:119], v[160:163], v[148:151], v[116:119]
	s_add_i32 s15, s3, 0xffffe000
	buffer_load_dwordx4 v[250:253], v173, s[8:11], s15 offen
	v_mfma_f32_16x16x32_bf16 v[112:115], v[164:167], v[148:151], v[112:115]
	v_mfma_f32_16x16x32_bf16 v[60:63], v[168:171], v[148:151], v[60:63]
	v_mfma_f32_16x16x32_bf16 v[68:71], v[156:159], v[152:155], v[68:71]
	v_mfma_f32_16x16x32_bf16 v[72:75], v[160:163], v[152:155], v[72:75]
	v_mfma_f32_16x16x32_bf16 v[80:83], v[164:167], v[152:155], v[80:83]
	buffer_load_dwordx4 v[188:191], v173, s[8:11], s3 offen
	v_mfma_f32_16x16x32_bf16 v[238:241], v[168:171], v[152:155], v[56:59]
	s_waitcnt vmcnt(4)
	v_cvt_pk_bf16_f32 v36, v24, v32
	v_cvt_pk_bf16_f32 v37, v20, v28
	ds_write_b64 v3, v[36:37] offset:49152
	v_cvt_pk_bf16_f32 v36, v25, v33
	v_cvt_pk_bf16_f32 v37, v21, v29
	ds_write_b64 v194, v[36:37] offset:49280
	v_cvt_pk_bf16_f32 v36, v26, v34
	v_cvt_pk_bf16_f32 v37, v22, v30
	ds_write_b64 v195, v[36:37] offset:49408
	v_cvt_pk_bf16_f32 v36, v27, v35
	v_cvt_pk_bf16_f32 v37, v23, v31
	ds_write_b64 v196, v[36:37] offset:49536
	s_waitcnt lgkmcnt(0)
	s_barrier
	s_nop 0
	v_mfma_f32_16x16x32_bf16 v[156:159], v[234:237], v[202:205], v[92:95]
	ds_read_b128 v[92:95], v176 offset:0
	v_mfma_f32_16x16x32_bf16 v[140:143], v[234:237], v[206:209], v[76:79]
	ds_read_b128 v[76:79], v176 offset:0x2000
	v_mfma_f32_16x16x32_bf16 v[136:139], v[222:225], v[210:213], v[124:127]
	v_mfma_f32_16x16x32_bf16 v[124:127], v[234:237], v[210:213], v[64:67]
	s_mov_b32 m0, s99
	s_add_i32 s15, s14, 0xfff80000
	buffer_load_dwordx4 v187, s[4:7], s15 offen lds
	ds_read_b128 v[64:67], v176 offset:0x4000
	v_mfma_f32_16x16x32_bf16 v[144:147], v[230:233], v[206:209], v[108:111]
	v_mfma_f32_16x16x32_bf16 v[108:111], v[234:237], v[214:217], v[60:63]
	ds_read_b128 v[60:63], v176 offset:0x6000
	ds_read_b128 v[56:59], v176 offset:0x8000
	v_mfma_f32_16x16x32_bf16 v[148:151], v[226:229], v[206:209], v[104:107]
	v_mfma_f32_16x16x32_bf16 v[104:107], v[222:225], v[218:221], v[68:71]
	s_add_i32 m0, s99, 0x2000
	s_add_i32 s65, s14, 0xfffa0000
	buffer_load_dwordx4 v187, s[4:7], s65 offen lds
	ds_read_b128 v[68:71], v178 offset:0
	v_mfma_f32_16x16x32_bf16 v[152:155], v[222:225], v[206:209], v[100:103]
	v_mfma_f32_16x16x32_bf16 v[100:103], v[226:229], v[218:221], v[72:75]
	ds_read_b128 v[72:75], v182 offset:0x800
	v_mfma_f32_16x16x32_bf16 v[168:171], v[222:225], v[202:205], v[84:87]
	v_mfma_f32_16x16x32_bf16 v[164:167], v[226:229], v[202:205], v[88:91]
	s_add_i32 m0, s99, 0x4000
	s_add_i32 s15, s14, 0xfffc0000
	buffer_load_dwordx4 v187, s[4:7], s15 offen lds
	v_mfma_f32_16x16x32_bf16 v[160:163], v[230:233], v[202:205], v[96:99]
	v_mfma_f32_16x16x32_bf16 v[132:135], v[226:229], v[210:213], v[132:135]
	v_mfma_f32_16x16x32_bf16 v[128:131], v[230:233], v[210:213], v[128:131]
	v_mfma_f32_16x16x32_bf16 v[120:123], v[222:225], v[214:217], v[120:123]
	s_add_i32 m0, s99, 0x6000
	s_add_i32 s65, s14, 0xfffe0000
	buffer_load_dwordx4 v187, s[4:7], s65 offen lds
	v_mfma_f32_16x16x32_bf16 v[116:119], v[226:229], v[214:217], v[116:119]
	v_mfma_f32_16x16x32_bf16 v[112:115], v[230:233], v[214:217], v[112:115]
	v_mfma_f32_16x16x32_bf16 v[96:99], v[230:233], v[218:221], v[80:83]
	ds_read_b128 v[80:83], v178 offset:0x1000
	ds_read_b128 v[84:87], v182 offset:0x1800
	v_mfma_f32_16x16x32_bf16 v[88:91], v[234:237], v[218:221], v[238:241]
	s_add_i32 m0, s99, 0x8000
	s_nop 0
	buffer_load_dwordx4 v187, s[4:7], s14 offen lds
	s_add_i32 s2, s2, 2
	s_add_i32 s3, s3, 0x100000
	s_addk_i32 s14, 0x100
	s_cmp_lt_u32 s2, 11
	s_cbranch_scc1 .LBB0_1430
	ds_read_b128 v[202:205], v180 offset:0
	ds_read_b128 v[206:209], v180 offset:0x2000
	ds_read_b128 v[210:213], v180 offset:0x4000
	ds_read_b128 v[214:217], v180 offset:0x6000
	ds_read_b128 v[218:221], v180 offset:0x8000
	ds_read_b128 v[222:225], v182 offset:0
	ds_read_b128 v[226:229], v178 offset:0x800
	ds_read_b128 v[230:233], v182 offset:0x1000
	ds_read_b128 v[234:237], v178 offset:0x1800
	s_waitcnt lgkmcnt(9)
	s_nop 0
	v_mfma_f32_16x16x32_bf16 v[168:171], v[68:71], v[92:95], v[168:171]
	v_mfma_f32_16x16x32_bf16 v[164:167], v[72:75], v[92:95], v[164:167]
	v_mfma_f32_16x16x32_bf16 v[160:163], v[80:83], v[92:95], v[160:163]
	v_mfma_f32_16x16x32_bf16 v[92:95], v[84:87], v[92:95], v[156:159]
	v_mfma_f32_16x16x32_bf16 v[152:155], v[68:71], v[76:79], v[152:155]
	v_mfma_f32_16x16x32_bf16 v[148:151], v[72:75], v[76:79], v[148:151]
	v_mfma_f32_16x16x32_bf16 v[144:147], v[80:83], v[76:79], v[144:147]
	v_mfma_f32_16x16x32_bf16 v[76:79], v[84:87], v[76:79], v[140:143]
	v_mfma_f32_16x16x32_bf16 v[136:139], v[68:71], v[64:67], v[136:139]
	v_mfma_f32_16x16x32_bf16 v[132:135], v[72:75], v[64:67], v[132:135]
	v_mfma_f32_16x16x32_bf16 v[128:131], v[80:83], v[64:67], v[128:131]
	v_mfma_f32_16x16x32_bf16 v[124:127], v[84:87], v[64:67], v[124:127]
	v_mfma_f32_16x16x32_bf16 v[120:123], v[68:71], v[60:63], v[120:123]
	v_mfma_f32_16x16x32_bf16 v[116:119], v[72:75], v[60:63], v[116:119]
	v_mfma_f32_16x16x32_bf16 v[112:115], v[80:83], v[60:63], v[112:115]
	v_mfma_f32_16x16x32_bf16 v[108:111], v[84:87], v[60:63], v[108:111]
	v_mfma_f32_16x16x32_bf16 v[104:107], v[68:71], v[56:59], v[104:107]
	v_mfma_f32_16x16x32_bf16 v[140:143], v[72:75], v[56:59], v[100:103]
	v_mfma_f32_16x16x32_bf16 v[156:159], v[80:83], v[56:59], v[96:99]
	v_mfma_f32_16x16x32_bf16 v[238:241], v[84:87], v[56:59], v[88:91]
	s_waitcnt vmcnt(0)
	v_cvt_pk_bf16_f32 v36, v242, v246
	v_cvt_pk_bf16_f32 v37, v250, v188
	ds_write_b64 v197, v[36:37]
	v_cvt_pk_bf16_f32 v36, v243, v247
	v_cvt_pk_bf16_f32 v37, v251, v189
	ds_write_b64 v198, v[36:37]
	v_cvt_pk_bf16_f32 v36, v244, v248
	v_cvt_pk_bf16_f32 v37, v252, v190
	ds_write_b64 v199, v[36:37]
	v_cvt_pk_bf16_f32 v36, v245, v249
	v_cvt_pk_bf16_f32 v37, v253, v191
	ds_write_b64 v200, v[36:37]
	s_waitcnt lgkmcnt(0)
	s_barrier
	s_nop 0
	v_mfma_f32_16x16x32_bf16 v[56:59], v[226:229], v[206:209], v[148:151]
	ds_read_b128 v[148:151], v177 offset:0
	v_mfma_f32_16x16x32_bf16 v[60:63], v[230:233], v[206:209], v[144:147]
	ds_read_b128 v[144:147], v177 offset:0x2000
	v_mfma_f32_16x16x32_bf16 v[80:83], v[234:237], v[210:213], v[124:127]
	ds_read_b128 v[124:127], v177 offset:0x4000
	v_mfma_f32_16x16x32_bf16 v[88:91], v[226:229], v[214:217], v[116:119]
	ds_read_b128 v[116:119], v177 offset:0x6000
	v_mfma_f32_16x16x32_bf16 v[96:99], v[234:237], v[214:217], v[108:111]
	ds_read_b128 v[108:111], v177 offset:0x8000
	v_mfma_f32_16x16x32_bf16 v[84:87], v[222:225], v[214:217], v[120:123]
	ds_read_b128 v[120:123], v179 offset:0
	v_mfma_f32_16x16x32_bf16 v[64:67], v[234:237], v[206:209], v[76:79]
	v_mfma_f32_16x16x32_bf16 v[76:79], v[230:233], v[210:213], v[128:131]
	ds_read_b128 v[128:131], v183 offset:0x800
	v_mfma_f32_16x16x32_bf16 v[20:23], v[222:225], v[202:205], v[168:171]
	v_mfma_f32_16x16x32_bf16 v[24:27], v[226:229], v[202:205], v[164:167]
	v_mfma_f32_16x16x32_bf16 v[28:31], v[230:233], v[202:205], v[160:163]
	v_mfma_f32_16x16x32_bf16 v[32:35], v[234:237], v[202:205], v[92:95]
	v_mfma_f32_16x16x32_bf16 v[52:55], v[222:225], v[206:209], v[152:155]
	v_mfma_f32_16x16x32_bf16 v[68:71], v[222:225], v[210:213], v[136:139]
	v_mfma_f32_16x16x32_bf16 v[72:75], v[226:229], v[210:213], v[132:135]
	ds_read_b128 v[132:135], v179 offset:0x1000
	ds_read_b128 v[136:139], v183 offset:0x1800
	v_mfma_f32_16x16x32_bf16 v[92:95], v[230:233], v[214:217], v[112:115]
	v_mfma_f32_16x16x32_bf16 v[100:103], v[222:225], v[218:221], v[104:107]
	v_mfma_f32_16x16x32_bf16 v[104:107], v[226:229], v[218:221], v[140:143]
	v_mfma_f32_16x16x32_bf16 v[112:115], v[230:233], v[218:221], v[156:159]
	v_mfma_f32_16x16x32_bf16 v[140:143], v[234:237], v[218:221], v[238:241]
	s_add_i32 s2, s63, 0x140
	s_cmp_ge_i32 s2, s54
	s_cselect_b64 s[2:3], -1, 0
	s_and_b64 s[2:3], s[20:21], s[2:3]
	v_mov_b64_e32 v[50:51], v[6:7]
	v_mov_b64_e32 v[46:47], v[10:11]
	v_mov_b64_e32 v[42:43], v[14:15]
	v_mov_b64_e32 v[38:39], v[18:19]
	s_andn2_b64 vcc, exec, s[2:3]
	v_mov_b64_e32 v[48:49], v[4:5]
	v_mov_b64_e32 v[44:45], v[8:9]
	v_mov_b64_e32 v[40:41], v[12:13]
	v_mov_b64_e32 v[36:37], v[16:17]
	s_cbranch_vccnz .LBB0_1433
	s_mov_b32 s14, s10
	s_mov_b32 s15, s11
	buffer_load_dwordx4 v[48:51], v173, s[12:15], 0 offen
	buffer_load_dwordx4 v[44:47], v173, s[12:15], s43 offen
	buffer_load_dwordx4 v[40:43], v173, s[12:15], s44 offen
	buffer_load_dwordx4 v[36:39], v173, s[12:15], s45 offen

.LBB0_1443:
	ds_read_b128 v[148:151], v180 offset:0
	ds_read_b128 v[152:155], v180 offset:0x2000
	ds_read_b128 v[156:159], v180 offset:0x4000
	ds_read_b128 v[160:163], v180 offset:0x6000
	ds_read_b128 v[164:167], v182 offset:0
	ds_read_b128 v[168:171], v178 offset:0x800
	ds_read_b128 v[202:205], v182 offset:0x1000
	ds_read_b128 v[206:209], v178 offset:0x1800
	s_waitcnt lgkmcnt(8)
	s_nop 1
	v_mfma_f32_16x16x32_bf16 v[144:147], v[64:67], v[72:75], v[144:147]
	v_mfma_f32_16x16x32_bf16 v[140:143], v[68:71], v[72:75], v[140:143]
	v_mfma_f32_16x16x32_bf16 v[136:139], v[76:79], v[72:75], v[136:139]
	v_mfma_f32_16x16x32_bf16 v[72:75], v[80:83], v[72:75], v[132:135]
	s_add_i32 s15, s3, 0xfff7a000
	buffer_load_dwordx4 v[24:27], v173, s[8:11], s15 offen
	v_mfma_f32_16x16x32_bf16 v[128:131], v[64:67], v[60:63], v[128:131]
	v_mfma_f32_16x16x32_bf16 v[124:127], v[68:71], v[60:63], v[124:127]
	v_mfma_f32_16x16x32_bf16 v[120:123], v[76:79], v[60:63], v[120:123]
	v_mfma_f32_16x16x32_bf16 v[60:63], v[80:83], v[60:63], v[116:119]
	s_add_i32 s23, s3, 0xfff7c000
	buffer_load_dwordx4 v[32:35], v173, s[8:11], s23 offen
	v_mfma_f32_16x16x32_bf16 v[112:115], v[64:67], v[56:59], v[112:115]
	v_mfma_f32_16x16x32_bf16 v[108:111], v[68:71], v[56:59], v[108:111]
	v_mfma_f32_16x16x32_bf16 v[104:107], v[76:79], v[56:59], v[104:107]
	v_mfma_f32_16x16x32_bf16 v[56:59], v[80:83], v[56:59], v[100:103]
	s_add_i32 s15, s3, 0xfff7e000
	buffer_load_dwordx4 v[20:23], v173, s[8:11], s15 offen
	v_mfma_f32_16x16x32_bf16 v[64:67], v[64:67], v[52:55], v[96:99]
	v_mfma_f32_16x16x32_bf16 v[68:71], v[68:71], v[52:55], v[92:95]
	v_mfma_f32_16x16x32_bf16 v[76:79], v[76:79], v[52:55], v[88:91]
	v_mfma_f32_16x16x32_bf16 v[52:55], v[80:83], v[52:55], v[84:87]
	s_add_i32 s23, s3, 0xfff80000
	buffer_load_dwordx4 v[28:31], v173, s[8:11], s23 offen
	s_waitcnt vmcnt(4)
	v_cvt_pk_bf16_f32 v36, v242, v246
	v_cvt_pk_bf16_f32 v37, v250, v188
	ds_write_b64 v197, v[36:37]
	v_cvt_pk_bf16_f32 v36, v243, v247
	v_cvt_pk_bf16_f32 v37, v251, v189
	ds_write_b64 v198, v[36:37]
	v_cvt_pk_bf16_f32 v36, v244, v248
	v_cvt_pk_bf16_f32 v37, v252, v190
	ds_write_b64 v199, v[36:37]
	v_cvt_pk_bf16_f32 v36, v245, v249
	v_cvt_pk_bf16_f32 v37, v253, v191
	ds_write_b64 v200, v[36:37]
	s_waitcnt lgkmcnt(0)
	s_barrier
	ds_read_b128 v[116:119], v177 offset:0
	s_nop 0
	v_mfma_f32_16x16x32_bf16 v[100:103], v[202:205], v[152:155], v[120:123]
	ds_read_b128 v[120:123], v177 offset:0x2000
	v_mfma_f32_16x16x32_bf16 v[96:99], v[168:171], v[152:155], v[124:127]
	ds_read_b128 v[124:127], v177 offset:0x4000
	v_mfma_f32_16x16x32_bf16 v[92:95], v[164:167], v[152:155], v[128:131]
	ds_read_b128 v[128:131], v177 offset:0x6000
	ds_read_b128 v[132:135], v179 offset:0
	v_mfma_f32_16x16x32_bf16 v[88:91], v[202:205], v[148:151], v[136:139]
	s_mov_b32 m0, s98
	s_add_i32 s15, s14, 0xfff9ff80
	buffer_load_dwordx4 v187, s[4:7], s15 offen lds
	ds_read_b128 v[136:139], v183 offset:0x800
	v_mfma_f32_16x16x32_bf16 v[80:83], v[164:167], v[148:151], v[144:147]
	v_mfma_f32_16x16x32_bf16 v[84:87], v[168:171], v[148:151], v[140:143]
	ds_read_b128 v[140:143], v179 offset:0x1000
	ds_read_b128 v[144:147], v183 offset:0x1800
	v_mfma_f32_16x16x32_bf16 v[72:75], v[206:209], v[148:151], v[72:75]
	v_mfma_f32_16x16x32_bf16 v[60:63], v[206:209], v[152:155], v[60:63]
	s_add_i32 m0, s98, 0x2000
	s_add_i32 s23, s14, 0xfffbff80
	buffer_load_dwordx4 v187, s[4:7], s23 offen lds
	v_mfma_f32_16x16x32_bf16 v[112:115], v[164:167], v[156:159], v[112:115]
	v_mfma_f32_16x16x32_bf16 v[108:111], v[168:171], v[156:159], v[108:111]
	v_mfma_f32_16x16x32_bf16 v[104:107], v[202:205], v[156:159], v[104:107]
	v_mfma_f32_16x16x32_bf16 v[56:59], v[206:209], v[156:159], v[56:59]
	s_add_i32 m0, s98, 0x4000
	s_add_i32 s15, s14, 0xfffdff80
	buffer_load_dwordx4 v187, s[4:7], s15 offen lds
	v_mfma_f32_16x16x32_bf16 v[64:67], v[164:167], v[160:163], v[64:67]
	v_mfma_f32_16x16x32_bf16 v[68:71], v[168:171], v[160:163], v[68:71]
	v_mfma_f32_16x16x32_bf16 v[76:79], v[202:205], v[160:163], v[76:79]
	v_mfma_f32_16x16x32_bf16 v[52:55], v[206:209], v[160:163], v[52:55]
	s_add_i32 m0, s98, 0x6000
	s_add_i32 s23, s14, 0xffffff80
	buffer_load_dwordx4 v187, s[4:7], s23 offen lds
	ds_read_b128 v[148:151], v181 offset:0
	ds_read_b128 v[152:155], v181 offset:0x2000
	ds_read_b128 v[156:159], v181 offset:0x4000
	ds_read_b128 v[160:163], v181 offset:0x6000
	ds_read_b128 v[164:167], v183 offset:0
	ds_read_b128 v[168:171], v179 offset:0x800
	ds_read_b128 v[202:205], v183 offset:0x1000
	ds_read_b128 v[206:209], v179 offset:0x1800
	s_waitcnt lgkmcnt(8)
	s_nop 0
	v_mfma_f32_16x16x32_bf16 v[80:83], v[132:135], v[116:119], v[80:83]
	v_mfma_f32_16x16x32_bf16 v[84:87], v[136:139], v[116:119], v[84:87]
	v_mfma_f32_16x16x32_bf16 v[88:91], v[140:143], v[116:119], v[88:91]
	v_mfma_f32_16x16x32_bf16 v[72:75], v[144:147], v[116:119], v[72:75]
	s_add_i32 s15, s3, 0xffffa000
	buffer_load_dwordx4 v[242:245], v173, s[8:11], s15 offen
	v_mfma_f32_16x16x32_bf16 v[92:95], v[132:135], v[120:123], v[92:95]
	v_mfma_f32_16x16x32_bf16 v[96:99], v[136:139], v[120:123], v[96:99]
	v_mfma_f32_16x16x32_bf16 v[100:103], v[140:143], v[120:123], v[100:103]
	v_mfma_f32_16x16x32_bf16 v[60:63], v[144:147], v[120:123], v[60:63]
	s_add_i32 s23, s3, 0xffffc000
	buffer_load_dwordx4 v[246:249], v173, s[8:11], s23 offen
	v_mfma_f32_16x16x32_bf16 v[112:115], v[132:135], v[124:127], v[112:115]
	v_mfma_f32_16x16x32_bf16 v[108:111], v[136:139], v[124:127], v[108:111]
	v_mfma_f32_16x16x32_bf16 v[104:107], v[140:143], v[124:127], v[104:107]
	v_mfma_f32_16x16x32_bf16 v[56:59], v[144:147], v[124:127], v[56:59]
	s_add_i32 s15, s3, 0xffffe000
	buffer_load_dwordx4 v[250:253], v173, s[8:11], s15 offen
	v_mfma_f32_16x16x32_bf16 v[64:67], v[132:135], v[128:131], v[64:67]
	v_mfma_f32_16x16x32_bf16 v[68:71], v[136:139], v[128:131], v[68:71]
	v_mfma_f32_16x16x32_bf16 v[76:79], v[140:143], v[128:131], v[76:79]
	v_mfma_f32_16x16x32_bf16 v[210:213], v[144:147], v[128:131], v[52:55]
	buffer_load_dwordx4 v[188:191], v173, s[8:11], s3 offen
	s_waitcnt vmcnt(4)
	v_cvt_pk_bf16_f32 v36, v24, v32
	v_cvt_pk_bf16_f32 v37, v20, v28
	ds_write_b64 v3, v[36:37] offset:49152
	v_cvt_pk_bf16_f32 v36, v25, v33
	v_cvt_pk_bf16_f32 v37, v21, v29
	ds_write_b64 v194, v[36:37] offset:49280
	v_cvt_pk_bf16_f32 v36, v26, v34
	v_cvt_pk_bf16_f32 v37, v22, v30
	ds_write_b64 v195, v[36:37] offset:49408
	v_cvt_pk_bf16_f32 v36, v27, v35
	v_cvt_pk_bf16_f32 v37, v23, v31
	ds_write_b64 v196, v[36:37] offset:49536
	s_waitcnt lgkmcnt(0)
	s_barrier
	s_nop 0
	v_mfma_f32_16x16x32_bf16 v[132:135], v[206:209], v[148:151], v[72:75]
	ds_read_b128 v[72:75], v176 offset:0
	v_mfma_f32_16x16x32_bf16 v[116:119], v[206:209], v[152:155], v[60:63]
	ds_read_b128 v[60:63], v176 offset:0x2000
	v_mfma_f32_16x16x32_bf16 v[120:123], v[202:205], v[152:155], v[100:103]
	v_mfma_f32_16x16x32_bf16 v[100:103], v[206:209], v[156:159], v[56:59]
	s_mov_b32 m0, s99
	s_add_i32 s15, s14, 0xfffa0000
	buffer_load_dwordx4 v187, s[4:7], s15 offen lds
	ds_read_b128 v[56:59], v176 offset:0x4000
	ds_read_b128 v[52:55], v176 offset:0x6000
	v_mfma_f32_16x16x32_bf16 v[124:127], v[168:171], v[152:155], v[96:99]
	v_mfma_f32_16x16x32_bf16 v[96:99], v[164:167], v[160:163], v[64:67]
	ds_read_b128 v[64:67], v178 offset:0
	v_mfma_f32_16x16x32_bf16 v[128:131], v[164:167], v[152:155], v[92:95]
	v_mfma_f32_16x16x32_bf16 v[92:95], v[168:171], v[160:163], v[68:71]
	s_add_i32 m0, s99, 0x2000
	s_add_i32 s23, s14, 0xfffc0000
	buffer_load_dwordx4 v187, s[4:7], s23 offen lds
	ds_read_b128 v[68:71], v182 offset:0x800
	v_mfma_f32_16x16x32_bf16 v[144:147], v[164:167], v[148:151], v[80:83]
	v_mfma_f32_16x16x32_bf16 v[140:143], v[168:171], v[148:151], v[84:87]
	v_mfma_f32_16x16x32_bf16 v[136:139], v[202:205], v[148:151], v[88:91]
	v_mfma_f32_16x16x32_bf16 v[112:115], v[164:167], v[156:159], v[112:115]
	s_add_i32 m0, s99, 0x4000
	s_add_i32 s15, s14, 0xfffe0000
	buffer_load_dwordx4 v187, s[4:7], s15 offen lds
	v_mfma_f32_16x16x32_bf16 v[108:111], v[168:171], v[156:159], v[108:111]
	v_mfma_f32_16x16x32_bf16 v[104:107], v[202:205], v[156:159], v[104:107]
	v_mfma_f32_16x16x32_bf16 v[88:91], v[202:205], v[160:163], v[76:79]
	ds_read_b128 v[76:79], v178 offset:0x1000
	ds_read_b128 v[80:83], v182 offset:0x1800
	v_mfma_f32_16x16x32_bf16 v[84:87], v[206:209], v[160:163], v[210:213]
	s_add_i32 m0, s99, 0x6000
	s_nop 0
	buffer_load_dwordx4 v187, s[4:7], s14 offen lds
	s_add_i32 s2, s2, 2
	s_add_i32 s3, s3, 0x100000
	s_addk_i32 s14, 0x100
	s_cmp_lt_u32 s2, 11
	s_cbranch_scc1 .LBB0_1443
	ds_read_b128 v[148:151], v180 offset:0
	ds_read_b128 v[152:155], v180 offset:0x2000
	ds_read_b128 v[156:159], v180 offset:0x4000
	ds_read_b128 v[160:163], v180 offset:0x6000
	ds_read_b128 v[164:167], v182 offset:0
	ds_read_b128 v[168:171], v178 offset:0x800
	ds_read_b128 v[202:205], v182 offset:0x1000
	ds_read_b128 v[206:209], v178 offset:0x1800
	s_waitcnt lgkmcnt(8)
	s_nop 0
	v_mfma_f32_16x16x32_bf16 v[144:147], v[64:67], v[72:75], v[144:147]
	v_mfma_f32_16x16x32_bf16 v[140:143], v[68:71], v[72:75], v[140:143]
	v_mfma_f32_16x16x32_bf16 v[136:139], v[76:79], v[72:75], v[136:139]
	v_mfma_f32_16x16x32_bf16 v[72:75], v[80:83], v[72:75], v[132:135]
	v_mfma_f32_16x16x32_bf16 v[128:131], v[64:67], v[60:63], v[128:131]
	v_mfma_f32_16x16x32_bf16 v[124:127], v[68:71], v[60:63], v[124:127]
	v_mfma_f32_16x16x32_bf16 v[120:123], v[76:79], v[60:63], v[120:123]
	v_mfma_f32_16x16x32_bf16 v[60:63], v[80:83], v[60:63], v[116:119]
	v_mfma_f32_16x16x32_bf16 v[112:115], v[64:67], v[56:59], v[112:115]
	v_mfma_f32_16x16x32_bf16 v[108:111], v[68:71], v[56:59], v[108:111]
	v_mfma_f32_16x16x32_bf16 v[104:107], v[76:79], v[56:59], v[104:107]
	v_mfma_f32_16x16x32_bf16 v[100:103], v[80:83], v[56:59], v[100:103]
	v_mfma_f32_16x16x32_bf16 v[96:99], v[64:67], v[52:55], v[96:99]
	v_mfma_f32_16x16x32_bf16 v[116:119], v[68:71], v[52:55], v[92:95]
	v_mfma_f32_16x16x32_bf16 v[132:135], v[76:79], v[52:55], v[88:91]
	v_mfma_f32_16x16x32_bf16 v[210:213], v[80:83], v[52:55], v[84:87]
	s_waitcnt vmcnt(0)
	v_cvt_pk_bf16_f32 v36, v242, v246
	v_cvt_pk_bf16_f32 v37, v250, v188
	ds_write_b64 v197, v[36:37]
	v_cvt_pk_bf16_f32 v36, v243, v247
	v_cvt_pk_bf16_f32 v37, v251, v189
	ds_write_b64 v198, v[36:37]
	v_cvt_pk_bf16_f32 v36, v244, v248
	v_cvt_pk_bf16_f32 v37, v252, v190
	ds_write_b64 v199, v[36:37]
	v_cvt_pk_bf16_f32 v36, v245, v249
	v_cvt_pk_bf16_f32 v37, v253, v191
	ds_write_b64 v200, v[36:37]
	s_waitcnt lgkmcnt(0)
	s_barrier
	s_nop 0
	v_mfma_f32_16x16x32_bf16 v[52:55], v[164:167], v[156:159], v[112:115]
	ds_read_b128 v[112:115], v177 offset:0
	ds_read_b128 v[92:95], v177 offset:0x2000
	ds_read_b128 v[84:87], v177 offset:0x4000
	ds_read_b128 v[76:79], v177 offset:0x6000
	ds_read_b128 v[88:91], v179 offset:0
	v_mfma_f32_16x16x32_bf16 v[68:71], v[164:167], v[160:163], v[96:99]
	ds_read_b128 v[96:99], v183 offset:0x800
	v_mfma_f32_16x16x32_bf16 v[20:23], v[164:167], v[148:151], v[144:147]
	v_mfma_f32_16x16x32_bf16 v[24:27], v[168:171], v[148:151], v[140:143]
	v_mfma_f32_16x16x32_bf16 v[28:31], v[202:205], v[148:151], v[136:139]
	v_mfma_f32_16x16x32_bf16 v[32:35], v[206:209], v[148:151], v[72:75]
	v_mfma_f32_16x16x32_bf16 v[36:39], v[164:167], v[152:155], v[128:131]
	v_mfma_f32_16x16x32_bf16 v[40:43], v[168:171], v[152:155], v[124:127]
	v_mfma_f32_16x16x32_bf16 v[44:47], v[202:205], v[152:155], v[120:123]
	v_mfma_f32_16x16x32_bf16 v[48:51], v[206:209], v[152:155], v[60:63]
	v_mfma_f32_16x16x32_bf16 v[56:59], v[168:171], v[156:159], v[108:111]
	v_mfma_f32_16x16x32_bf16 v[60:63], v[202:205], v[156:159], v[104:107]
	v_mfma_f32_16x16x32_bf16 v[64:67], v[206:209], v[156:159], v[100:103]
	ds_read_b128 v[100:103], v179 offset:0x1000
	ds_read_b128 v[104:107], v183 offset:0x1800
	v_mfma_f32_16x16x32_bf16 v[72:75], v[168:171], v[160:163], v[116:119]
	v_mfma_f32_16x16x32_bf16 v[80:83], v[202:205], v[160:163], v[132:135]
	v_mfma_f32_16x16x32_bf16 v[108:111], v[206:209], v[160:163], v[210:213]
	s_andn2_b64 vcc, exec, s[20:21]
	s_cbranch_vccnz .LBB0_1446
	s_mov_b32 s14, s10
	s_mov_b32 s15, s11
	buffer_load_dwordx4 v[4:7], v173, s[12:15], 0 offen
	buffer_load_dwordx4 v[8:11], v173, s[12:15], s43 offen
	buffer_load_dwordx4 v[12:15], v173, s[12:15], s44 offen
	buffer_load_dwordx4 v[16:19], v173, s[12:15], s45 offen
